# LN kernels: 6-step ds_bpermute butterfly replaced by DPP adds + readlane for the wave reduction (shorter post-load latency chain)
# speedup vs baseline: 1.0193x; 1.0024x over previous
.Lln00_noys:
	s_cmp_eq_u32 s25, 0
	s_cbranch_scc1 .Lln00_end
	v_add_f32_e32 v4, v44, v45
	v_add_f32_e32 v5, v48, v49
	v_add_f32_e32 v4, v46, v4
	v_add_f32_e32 v5, v50, v5
	v_add_f32_e32 v4, v47, v4
	v_add_f32_e32 v5, v51, v5
	v_add_f32_e32 v4, 0, v4
	v_add_f32_e32 v4, v4, v5
	s_nop 1
	v_add_f32_dpp v5, v4, v4 quad_perm:[1,0,3,2] row_mask:0xf bank_mask:0xf
	s_nop 1
	v_add_f32_dpp v4, v5, v5 quad_perm:[2,3,0,1] row_mask:0xf bank_mask:0xf
	s_nop 1
	v_add_f32_dpp v5, v4, v4 row_ror:4 row_mask:0xf bank_mask:0xf
	s_nop 1
	v_add_f32_dpp v4, v5, v5 row_ror:8 row_mask:0xf bank_mask:0xf
	s_nop 1
	v_add_f32_dpp v4, v4, v4 row_bcast:15 row_mask:0xa bank_mask:0xf
	s_nop 1
	v_add_f32_dpp v4, v4, v4 row_bcast:31 row_mask:0xc bank_mask:0xf
	s_nop 1
	v_readlane_b32 s26, v4, 63
	s_nop 3
	v_mov_b32_e32 v4, s26
	v_cmp_eq_u32_e32 vcc, 0, v60
	s_and_saveexec_b64 s[26:27], vcc
	ds_write_b32 v61, v4
	s_or_b64 exec, exec, s[26:27]
	v_mov_b32_e32 v9, 0
	s_waitcnt lgkmcnt(0)
	s_barrier
	ds_read_b128 v[4:7], v9
	s_waitcnt lgkmcnt(0)
	s_barrier
	v_add_f32_e32 v8, v4, v5
	v_add_f32_e32 v8, v8, v6
	v_add_f32_e32 v8, v8, v7
	v_mul_f32_e32 v10, 0x3a000000, v8
	s_nop 0
	v_pk_add_f32 v[44:45], v[44:45], v[10:11] op_sel_hi:[1,0] neg_lo:[0,1] neg_hi:[0,1]
	v_pk_add_f32 v[46:47], v[46:47], v[10:11] op_sel_hi:[1,0] neg_lo:[0,1] neg_hi:[0,1]
	v_pk_add_f32 v[48:49], v[48:49], v[10:11] op_sel_hi:[1,0] neg_lo:[0,1] neg_hi:[0,1]
	v_pk_add_f32 v[50:51], v[50:51], v[10:11] op_sel_hi:[1,0] neg_lo:[0,1] neg_hi:[0,1]
	s_nop 0
	v_pk_mul_f32 v[12:13], v[44:45], v[44:45]
	v_pk_mul_f32 v[14:15], v[46:47], v[46:47]
	v_pk_mul_f32 v[16:17], v[48:49], v[48:49]
	v_pk_mul_f32 v[18:19], v[50:51], v[50:51]
	v_add_f32_e32 v4, v12, v13
	v_add_f32_e32 v4, v4, v14
	v_add_f32_e32 v4, v4, v15
	v_add_f32_e32 v4, v4, v16
	v_add_f32_e32 v4, v4, v17
	v_add_f32_e32 v4, v4, v18
	v_add_f32_e32 v4, v4, v19
	s_nop 1
	v_add_f32_dpp v5, v4, v4 quad_perm:[1,0,3,2] row_mask:0xf bank_mask:0xf
	s_nop 1
	v_add_f32_dpp v4, v5, v5 quad_perm:[2,3,0,1] row_mask:0xf bank_mask:0xf
	s_nop 1
	v_add_f32_dpp v5, v4, v4 row_ror:4 row_mask:0xf bank_mask:0xf
	s_nop 1
	v_add_f32_dpp v4, v5, v5 row_ror:8 row_mask:0xf bank_mask:0xf
	s_nop 1
	v_add_f32_dpp v4, v4, v4 row_bcast:15 row_mask:0xa bank_mask:0xf
	s_nop 1
	v_add_f32_dpp v4, v4, v4 row_bcast:31 row_mask:0xc bank_mask:0xf
	s_nop 1
	v_readlane_b32 s26, v4, 63
	s_nop 3
	v_mov_b32_e32 v4, s26
	v_cmp_eq_u32_e32 vcc, 0, v60
	s_and_saveexec_b64 s[26:27], vcc
	ds_write_b32 v61, v4
	s_or_b64 exec, exec, s[26:27]
	v_mov_b32_e32 v9, 0
	s_waitcnt lgkmcnt(0)
	s_barrier
	ds_read_b128 v[4:7], v9
	s_waitcnt lgkmcnt(0)
	v_add_f32_e32 v8, v4, v5
	v_add_f32_e32 v8, v8, v6
	v_add_f32_e32 v8, v8, v7
	v_mov_b32_e32 v10, 0x3727c5ac
	v_fmac_f32_e32 v10, 0x3a000000, v8
	s_mov_b32 s26, 0x800000
	v_mul_f32_e32 v12, 0x4b800000, v10
	v_cmp_gt_f32_e32 vcc, s26, v10
	s_nop 1
	v_cndmask_b32_e32 v12, v10, v12, vcc
	v_rsq_f32_e32 v12, v12
	s_nop 0
	v_mul_f32_e32 v14, 0x45800000, v12
	v_cndmask_b32_e32 v12, v12, v14, vcc
	s_nop 0
	v_pk_mul_f32 v[44:45], v[12:13], v[44:45] op_sel_hi:[0,1]
	v_pk_mul_f32 v[46:47], v[12:13], v[46:47] op_sel_hi:[0,1]
	v_pk_mul_f32 v[48:49], v[12:13], v[48:49] op_sel_hi:[0,1]
	v_pk_mul_f32 v[50:51], v[12:13], v[50:51] op_sel_hi:[0,1]
	s_waitcnt vmcnt(0)
	v_pk_fma_f32 v[44:45], v[28:29], v[44:45], v[36:37]
	v_pk_fma_f32 v[46:47], v[30:31], v[46:47], v[38:39]
	v_pk_fma_f32 v[48:49], v[32:33], v[48:49], v[40:41]
	v_pk_fma_f32 v[50:51], v[34:35], v[50:51], v[42:43]
	v_cvt_pk_f16_f32 v4, v44, v45
	v_cvt_pk_f16_f32 v5, v46, v47
	v_cvt_pk_f16_f32 v6, v48, v49
	v_cvt_pk_f16_f32 v7, v50, v51
	global_store_dwordx2 v1, v[4:5], s[14:15] sc1
	global_store_dwordx2 v1, v[6:7], s[14:15] offset:2048 sc1
